# speedup vs baseline: 1.0427x; 1.0139x over previous
.LBB2_114:
	s_setprio 0
	v_and_b32_e32 v0, 16, v0
	v_lshlrev_b32_e32 v1, 2, v191
	s_lshl_b32 s0, s34, 5
	v_add_u32_e32 v70, 12, v1
	v_cmp_eq_u32_e32 vcc, 0, v0
	s_add_i32 s0, s0, s33
	s_mov_b32 s1, 0x3f3504f3
	v_cndmask_b32_e32 v0, v70, v1, vcc
	v_or_b32_e32 v0, s0, v0
	v_ashrrev_i32_e32 v1, 31, v0
	v_lshl_add_u64 v[78:79], v[0:1], 1, s[4:5]
	s_waitcnt vmcnt(0) lgkmcnt(0)
	s_mov_b32 s76, 0x3e6d3388
	s_mov_b32 s78, 0xbf38aa3b
	s_mov_b32 s80, 0x3f87dc22
	s_mov_b32 s82, 0x3fb5f0e3
	s_mov_b32 s84, 0xbe91a98e
	s_mov_b32 s86, 0x3e827906
	v_mov_b32_e32 v248, 0xbfba00e3
	v_mov_b32_e32 v249, 0xbfba00e3
	v_mul_f32_e32 v232, 0.5, v220
	v_pk_mul_f32 v[234:235], v[74:75], v[74:75]
	v_fma_f32 v236, |v74|, s76, 1.0
	v_fma_f32 v237, |v75|, s76, 1.0
	v_pk_mul_f32 v[234:235], v[234:235], s[78:79] op_sel_hi:[1,0]
	v_rcp_f32_e32 v236, v236
	v_rcp_f32_e32 v237, v237
	v_exp_f32_e32 v234, v234
	v_exp_f32_e32 v235, v235
	v_pk_fma_f32 v[238:239], v[236:237], s[80:81], v[248:249] op_sel_hi:[1,0,1]
	v_pk_mul_f32 v[240:241], v[232:233], v[74:75] op_sel_hi:[0,1]
	v_pk_fma_f32 v[238:239], v[238:239], v[236:237], s[82:83] op_sel_hi:[1,1,0]
	s_nop 0
	v_pk_fma_f32 v[238:239], v[238:239], v[236:237], s[84:85] op_sel_hi:[1,1,0]
	s_nop 0
	v_pk_fma_f32 v[238:239], v[238:239], v[236:237], s[86:87] op_sel_hi:[1,1,0]
	s_nop 0
	v_pk_mul_f32 v[238:239], v[238:239], v[236:237]
	s_nop 0
	v_pk_fma_f32 v[238:239], v[238:239], v[234:235], 1.0 op_sel_hi:[1,1,0] neg_lo:[1,0,0] neg_hi:[1,0,0]
	s_nop 0
	v_fma_f32 v242, |v240|, v238, v240
	v_fma_f32 v243, |v241|, v239, v241
	v_cvt_pk_f16_f32 v244, v242, v243
	v_pk_mul_f32 v[234:235], v[76:77], v[76:77]
	v_fma_f32 v236, |v76|, s76, 1.0
	v_fma_f32 v237, |v77|, s76, 1.0
	v_pk_mul_f32 v[234:235], v[234:235], s[78:79] op_sel_hi:[1,0]
	v_rcp_f32_e32 v236, v236
	v_rcp_f32_e32 v237, v237
	v_exp_f32_e32 v234, v234
	v_exp_f32_e32 v235, v235
	v_pk_fma_f32 v[238:239], v[236:237], s[80:81], v[248:249] op_sel_hi:[1,0,1]
	v_pk_mul_f32 v[240:241], v[232:233], v[76:77] op_sel_hi:[0,1]
	v_pk_fma_f32 v[238:239], v[238:239], v[236:237], s[82:83] op_sel_hi:[1,1,0]
	s_nop 0
	v_pk_fma_f32 v[238:239], v[238:239], v[236:237], s[84:85] op_sel_hi:[1,1,0]
	s_nop 0
	v_pk_fma_f32 v[238:239], v[238:239], v[236:237], s[86:87] op_sel_hi:[1,1,0]
	s_nop 0
	v_pk_mul_f32 v[238:239], v[238:239], v[236:237]
	s_nop 0
	v_pk_fma_f32 v[238:239], v[238:239], v[234:235], 1.0 op_sel_hi:[1,1,0] neg_lo:[1,0,0] neg_hi:[1,0,0]
	s_nop 0
	v_fma_f32 v242, |v240|, v238, v240
	v_fma_f32 v243, |v241|, v239, v241
	v_cvt_pk_f16_f32 v245, v242, v243
	v_pk_mul_f32 v[234:235], v[66:67], v[66:67]
	v_fma_f32 v236, |v66|, s76, 1.0
	v_fma_f32 v237, |v67|, s76, 1.0
	v_pk_mul_f32 v[234:235], v[234:235], s[78:79] op_sel_hi:[1,0]
	v_rcp_f32_e32 v236, v236
	v_rcp_f32_e32 v237, v237
	v_exp_f32_e32 v234, v234
	v_exp_f32_e32 v235, v235
	v_pk_fma_f32 v[238:239], v[236:237], s[80:81], v[248:249] op_sel_hi:[1,0,1]
	v_pk_mul_f32 v[240:241], v[232:233], v[66:67] op_sel_hi:[0,1]
	v_pk_fma_f32 v[238:239], v[238:239], v[236:237], s[82:83] op_sel_hi:[1,1,0]
	s_nop 0
	v_pk_fma_f32 v[238:239], v[238:239], v[236:237], s[84:85] op_sel_hi:[1,1,0]
	s_nop 0
	v_pk_fma_f32 v[238:239], v[238:239], v[236:237], s[86:87] op_sel_hi:[1,1,0]
	s_nop 0
	v_pk_mul_f32 v[238:239], v[238:239], v[236:237]
	s_nop 0
	v_pk_fma_f32 v[238:239], v[238:239], v[234:235], 1.0 op_sel_hi:[1,1,0] neg_lo:[1,0,0] neg_hi:[1,0,0]
	s_nop 0
	v_fma_f32 v242, |v240|, v238, v240
	v_fma_f32 v243, |v241|, v239, v241
	v_cvt_pk_f16_f32 v246, v242, v243
	v_pk_mul_f32 v[234:235], v[68:69], v[68:69]
	v_fma_f32 v236, |v68|, s76, 1.0
	v_fma_f32 v237, |v69|, s76, 1.0
	v_pk_mul_f32 v[234:235], v[234:235], s[78:79] op_sel_hi:[1,0]
	v_rcp_f32_e32 v236, v236
	v_rcp_f32_e32 v237, v237
	v_exp_f32_e32 v234, v234
	v_exp_f32_e32 v235, v235
	v_pk_fma_f32 v[238:239], v[236:237], s[80:81], v[248:249] op_sel_hi:[1,0,1]
	v_pk_mul_f32 v[240:241], v[232:233], v[68:69] op_sel_hi:[0,1]
	v_pk_fma_f32 v[238:239], v[238:239], v[236:237], s[82:83] op_sel_hi:[1,1,0]
	s_nop 0
	v_pk_fma_f32 v[238:239], v[238:239], v[236:237], s[84:85] op_sel_hi:[1,1,0]
	s_nop 0
	v_pk_fma_f32 v[238:239], v[238:239], v[236:237], s[86:87] op_sel_hi:[1,1,0]
	s_nop 0
	v_pk_mul_f32 v[238:239], v[238:239], v[236:237]
	s_nop 0
	v_pk_fma_f32 v[238:239], v[238:239], v[234:235], 1.0 op_sel_hi:[1,1,0] neg_lo:[1,0,0] neg_hi:[1,0,0]
	s_nop 0
	v_fma_f32 v242, |v240|, v238, v240
	v_fma_f32 v243, |v241|, v239, v241
	v_cvt_pk_f16_f32 v247, v242, v243
	v_cmp_lt_i32_e32 vcc, -1, v218
	s_nop 0
	v_permlane16_swap_b32_e32 v244, v246
	v_permlane16_swap_b32_e32 v245, v247
	s_and_saveexec_b64 s[10:11], vcc
	s_cbranch_execz .Lep_0
	v_mov_b32_e32 v250, v218
	v_mov_b32_e32 v251, 0
	v_lshlrev_b64 v[250:251], 10, v[250:251]
	v_lshl_add_u64 v[250:251], v[78:79], 0, v[250:251]
	global_store_dwordx4 v[250:251], v[244:247], off sc1
.Lep_0:
	s_or_b64 exec, exec, s[10:11]
	v_mul_f32_e32 v232, 0.5, v216
	v_pk_mul_f32 v[234:235], v[62:63], v[62:63]
	v_fma_f32 v236, |v62|, s76, 1.0
	v_fma_f32 v237, |v63|, s76, 1.0
	v_pk_mul_f32 v[234:235], v[234:235], s[78:79] op_sel_hi:[1,0]
	v_rcp_f32_e32 v236, v236
	v_rcp_f32_e32 v237, v237
	v_exp_f32_e32 v234, v234
	v_exp_f32_e32 v235, v235
	v_pk_fma_f32 v[238:239], v[236:237], s[80:81], v[248:249] op_sel_hi:[1,0,1]
	v_pk_mul_f32 v[240:241], v[232:233], v[62:63] op_sel_hi:[0,1]
	v_pk_fma_f32 v[238:239], v[238:239], v[236:237], s[82:83] op_sel_hi:[1,1,0]
	s_nop 0
	v_pk_fma_f32 v[238:239], v[238:239], v[236:237], s[84:85] op_sel_hi:[1,1,0]
	s_nop 0
	v_pk_fma_f32 v[238:239], v[238:239], v[236:237], s[86:87] op_sel_hi:[1,1,0]
	s_nop 0
	v_pk_mul_f32 v[238:239], v[238:239], v[236:237]
	s_nop 0
	v_pk_fma_f32 v[238:239], v[238:239], v[234:235], 1.0 op_sel_hi:[1,1,0] neg_lo:[1,0,0] neg_hi:[1,0,0]
	s_nop 0
	v_fma_f32 v242, |v240|, v238, v240
	v_fma_f32 v243, |v241|, v239, v241
	v_cvt_pk_f16_f32 v244, v242, v243
	v_pk_mul_f32 v[234:235], v[64:65], v[64:65]
	v_fma_f32 v236, |v64|, s76, 1.0
	v_fma_f32 v237, |v65|, s76, 1.0
	v_pk_mul_f32 v[234:235], v[234:235], s[78:79] op_sel_hi:[1,0]
	v_rcp_f32_e32 v236, v236
	v_rcp_f32_e32 v237, v237
	v_exp_f32_e32 v234, v234
	v_exp_f32_e32 v235, v235
	v_pk_fma_f32 v[238:239], v[236:237], s[80:81], v[248:249] op_sel_hi:[1,0,1]
	v_pk_mul_f32 v[240:241], v[232:233], v[64:65] op_sel_hi:[0,1]
	v_pk_fma_f32 v[238:239], v[238:239], v[236:237], s[82:83] op_sel_hi:[1,1,0]
	s_nop 0
	v_pk_fma_f32 v[238:239], v[238:239], v[236:237], s[84:85] op_sel_hi:[1,1,0]
	s_nop 0
	v_pk_fma_f32 v[238:239], v[238:239], v[236:237], s[86:87] op_sel_hi:[1,1,0]
	s_nop 0
	v_pk_mul_f32 v[238:239], v[238:239], v[236:237]
	s_nop 0
	v_pk_fma_f32 v[238:239], v[238:239], v[234:235], 1.0 op_sel_hi:[1,1,0] neg_lo:[1,0,0] neg_hi:[1,0,0]
	s_nop 0
	v_fma_f32 v242, |v240|, v238, v240
	v_fma_f32 v243, |v241|, v239, v241
	v_cvt_pk_f16_f32 v245, v242, v243
	v_pk_mul_f32 v[234:235], v[58:59], v[58:59]
	v_fma_f32 v236, |v58|, s76, 1.0
	v_fma_f32 v237, |v59|, s76, 1.0
	v_pk_mul_f32 v[234:235], v[234:235], s[78:79] op_sel_hi:[1,0]
	v_rcp_f32_e32 v236, v236
	v_rcp_f32_e32 v237, v237
	v_exp_f32_e32 v234, v234
	v_exp_f32_e32 v235, v235
	v_pk_fma_f32 v[238:239], v[236:237], s[80:81], v[248:249] op_sel_hi:[1,0,1]
	v_pk_mul_f32 v[240:241], v[232:233], v[58:59] op_sel_hi:[0,1]
	v_pk_fma_f32 v[238:239], v[238:239], v[236:237], s[82:83] op_sel_hi:[1,1,0]
	s_nop 0
	v_pk_fma_f32 v[238:239], v[238:239], v[236:237], s[84:85] op_sel_hi:[1,1,0]
	s_nop 0
	v_pk_fma_f32 v[238:239], v[238:239], v[236:237], s[86:87] op_sel_hi:[1,1,0]
	s_nop 0
	v_pk_mul_f32 v[238:239], v[238:239], v[236:237]
	s_nop 0
	v_pk_fma_f32 v[238:239], v[238:239], v[234:235], 1.0 op_sel_hi:[1,1,0] neg_lo:[1,0,0] neg_hi:[1,0,0]
	s_nop 0
	v_fma_f32 v242, |v240|, v238, v240
	v_fma_f32 v243, |v241|, v239, v241
	v_cvt_pk_f16_f32 v246, v242, v243
	v_pk_mul_f32 v[234:235], v[60:61], v[60:61]
	v_fma_f32 v236, |v60|, s76, 1.0
	v_fma_f32 v237, |v61|, s76, 1.0
	v_pk_mul_f32 v[234:235], v[234:235], s[78:79] op_sel_hi:[1,0]
	v_rcp_f32_e32 v236, v236
	v_rcp_f32_e32 v237, v237
	v_exp_f32_e32 v234, v234
	v_exp_f32_e32 v235, v235
	v_pk_fma_f32 v[238:239], v[236:237], s[80:81], v[248:249] op_sel_hi:[1,0,1]
	v_pk_mul_f32 v[240:241], v[232:233], v[60:61] op_sel_hi:[0,1]
	v_pk_fma_f32 v[238:239], v[238:239], v[236:237], s[82:83] op_sel_hi:[1,1,0]
	s_nop 0
	v_pk_fma_f32 v[238:239], v[238:239], v[236:237], s[84:85] op_sel_hi:[1,1,0]
	s_nop 0
	v_pk_fma_f32 v[238:239], v[238:239], v[236:237], s[86:87] op_sel_hi:[1,1,0]
	s_nop 0
	v_pk_mul_f32 v[238:239], v[238:239], v[236:237]
	s_nop 0
	v_pk_fma_f32 v[238:239], v[238:239], v[234:235], 1.0 op_sel_hi:[1,1,0] neg_lo:[1,0,0] neg_hi:[1,0,0]
	s_nop 0
	v_fma_f32 v242, |v240|, v238, v240
	v_fma_f32 v243, |v241|, v239, v241
	v_cvt_pk_f16_f32 v247, v242, v243
	v_cmp_lt_i32_e32 vcc, -1, v214
	s_nop 0
	v_permlane16_swap_b32_e32 v244, v246
	v_permlane16_swap_b32_e32 v245, v247
	s_and_saveexec_b64 s[10:11], vcc
	s_cbranch_execz .Lep_1
	v_mov_b32_e32 v250, v214
	v_mov_b32_e32 v251, 0
	v_lshlrev_b64 v[250:251], 10, v[250:251]
	v_lshl_add_u64 v[250:251], v[78:79], 0, v[250:251]
	global_store_dwordx4 v[250:251], v[244:247], off sc1
.Lep_1:
	s_or_b64 exec, exec, s[10:11]
	v_mul_f32_e32 v232, 0.5, v212
	v_pk_mul_f32 v[234:235], v[54:55], v[54:55]
	v_fma_f32 v236, |v54|, s76, 1.0
	v_fma_f32 v237, |v55|, s76, 1.0
	v_pk_mul_f32 v[234:235], v[234:235], s[78:79] op_sel_hi:[1,0]
	v_rcp_f32_e32 v236, v236
	v_rcp_f32_e32 v237, v237
	v_exp_f32_e32 v234, v234
	v_exp_f32_e32 v235, v235
	v_pk_fma_f32 v[238:239], v[236:237], s[80:81], v[248:249] op_sel_hi:[1,0,1]
	v_pk_mul_f32 v[240:241], v[232:233], v[54:55] op_sel_hi:[0,1]
	v_pk_fma_f32 v[238:239], v[238:239], v[236:237], s[82:83] op_sel_hi:[1,1,0]
	s_nop 0
	v_pk_fma_f32 v[238:239], v[238:239], v[236:237], s[84:85] op_sel_hi:[1,1,0]
	s_nop 0
	v_pk_fma_f32 v[238:239], v[238:239], v[236:237], s[86:87] op_sel_hi:[1,1,0]
	s_nop 0
	v_pk_mul_f32 v[238:239], v[238:239], v[236:237]
	s_nop 0
	v_pk_fma_f32 v[238:239], v[238:239], v[234:235], 1.0 op_sel_hi:[1,1,0] neg_lo:[1,0,0] neg_hi:[1,0,0]
	s_nop 0
	v_fma_f32 v242, |v240|, v238, v240
	v_fma_f32 v243, |v241|, v239, v241
	v_cvt_pk_f16_f32 v244, v242, v243
	v_pk_mul_f32 v[234:235], v[56:57], v[56:57]
	v_fma_f32 v236, |v56|, s76, 1.0
	v_fma_f32 v237, |v57|, s76, 1.0
	v_pk_mul_f32 v[234:235], v[234:235], s[78:79] op_sel_hi:[1,0]
	v_rcp_f32_e32 v236, v236
	v_rcp_f32_e32 v237, v237
	v_exp_f32_e32 v234, v234
	v_exp_f32_e32 v235, v235
	v_pk_fma_f32 v[238:239], v[236:237], s[80:81], v[248:249] op_sel_hi:[1,0,1]
	v_pk_mul_f32 v[240:241], v[232:233], v[56:57] op_sel_hi:[0,1]
	v_pk_fma_f32 v[238:239], v[238:239], v[236:237], s[82:83] op_sel_hi:[1,1,0]
	s_nop 0
	v_pk_fma_f32 v[238:239], v[238:239], v[236:237], s[84:85] op_sel_hi:[1,1,0]
	s_nop 0
	v_pk_fma_f32 v[238:239], v[238:239], v[236:237], s[86:87] op_sel_hi:[1,1,0]
	s_nop 0
	v_pk_mul_f32 v[238:239], v[238:239], v[236:237]
	s_nop 0
	v_pk_fma_f32 v[238:239], v[238:239], v[234:235], 1.0 op_sel_hi:[1,1,0] neg_lo:[1,0,0] neg_hi:[1,0,0]
	s_nop 0
	v_fma_f32 v242, |v240|, v238, v240
	v_fma_f32 v243, |v241|, v239, v241
	v_cvt_pk_f16_f32 v245, v242, v243
	v_pk_mul_f32 v[234:235], v[50:51], v[50:51]
	v_fma_f32 v236, |v50|, s76, 1.0
	v_fma_f32 v237, |v51|, s76, 1.0
	v_pk_mul_f32 v[234:235], v[234:235], s[78:79] op_sel_hi:[1,0]
	v_rcp_f32_e32 v236, v236
	v_rcp_f32_e32 v237, v237
	v_exp_f32_e32 v234, v234
	v_exp_f32_e32 v235, v235
	v_pk_fma_f32 v[238:239], v[236:237], s[80:81], v[248:249] op_sel_hi:[1,0,1]
	v_pk_mul_f32 v[240:241], v[232:233], v[50:51] op_sel_hi:[0,1]
	v_pk_fma_f32 v[238:239], v[238:239], v[236:237], s[82:83] op_sel_hi:[1,1,0]
	s_nop 0
	v_pk_fma_f32 v[238:239], v[238:239], v[236:237], s[84:85] op_sel_hi:[1,1,0]
	s_nop 0
	v_pk_fma_f32 v[238:239], v[238:239], v[236:237], s[86:87] op_sel_hi:[1,1,0]
	s_nop 0
	v_pk_mul_f32 v[238:239], v[238:239], v[236:237]
	s_nop 0
	v_pk_fma_f32 v[238:239], v[238:239], v[234:235], 1.0 op_sel_hi:[1,1,0] neg_lo:[1,0,0] neg_hi:[1,0,0]
	s_nop 0
	v_fma_f32 v242, |v240|, v238, v240
	v_fma_f32 v243, |v241|, v239, v241
	v_cvt_pk_f16_f32 v246, v242, v243
	v_pk_mul_f32 v[234:235], v[52:53], v[52:53]
	v_fma_f32 v236, |v52|, s76, 1.0
	v_fma_f32 v237, |v53|, s76, 1.0
	v_pk_mul_f32 v[234:235], v[234:235], s[78:79] op_sel_hi:[1,0]
	v_rcp_f32_e32 v236, v236
	v_rcp_f32_e32 v237, v237
	v_exp_f32_e32 v234, v234
	v_exp_f32_e32 v235, v235
	v_pk_fma_f32 v[238:239], v[236:237], s[80:81], v[248:249] op_sel_hi:[1,0,1]
	v_pk_mul_f32 v[240:241], v[232:233], v[52:53] op_sel_hi:[0,1]
	v_pk_fma_f32 v[238:239], v[238:239], v[236:237], s[82:83] op_sel_hi:[1,1,0]
	s_nop 0
	v_pk_fma_f32 v[238:239], v[238:239], v[236:237], s[84:85] op_sel_hi:[1,1,0]
	s_nop 0
	v_pk_fma_f32 v[238:239], v[238:239], v[236:237], s[86:87] op_sel_hi:[1,1,0]
	s_nop 0
	v_pk_mul_f32 v[238:239], v[238:239], v[236:237]
	s_nop 0
	v_pk_fma_f32 v[238:239], v[238:239], v[234:235], 1.0 op_sel_hi:[1,1,0] neg_lo:[1,0,0] neg_hi:[1,0,0]
	s_nop 0
	v_fma_f32 v242, |v240|, v238, v240
	v_fma_f32 v243, |v241|, v239, v241
	v_cvt_pk_f16_f32 v247, v242, v243
	v_cmp_lt_i32_e32 vcc, -1, v210
	s_nop 0
	v_permlane16_swap_b32_e32 v244, v246
	v_permlane16_swap_b32_e32 v245, v247
	s_and_saveexec_b64 s[10:11], vcc
	s_cbranch_execz .Lep_2
	v_mov_b32_e32 v250, v210
	v_mov_b32_e32 v251, 0
	v_lshlrev_b64 v[250:251], 10, v[250:251]
	v_lshl_add_u64 v[250:251], v[78:79], 0, v[250:251]
	global_store_dwordx4 v[250:251], v[244:247], off sc1
.Lep_2:
	s_or_b64 exec, exec, s[10:11]
	v_mul_f32_e32 v232, 0.5, v208
	v_pk_mul_f32 v[234:235], v[46:47], v[46:47]
	v_fma_f32 v236, |v46|, s76, 1.0
	v_fma_f32 v237, |v47|, s76, 1.0
	v_pk_mul_f32 v[234:235], v[234:235], s[78:79] op_sel_hi:[1,0]
	v_rcp_f32_e32 v236, v236
	v_rcp_f32_e32 v237, v237
	v_exp_f32_e32 v234, v234
	v_exp_f32_e32 v235, v235
	v_pk_fma_f32 v[238:239], v[236:237], s[80:81], v[248:249] op_sel_hi:[1,0,1]
	v_pk_mul_f32 v[240:241], v[232:233], v[46:47] op_sel_hi:[0,1]
	v_pk_fma_f32 v[238:239], v[238:239], v[236:237], s[82:83] op_sel_hi:[1,1,0]
	s_nop 0
	v_pk_fma_f32 v[238:239], v[238:239], v[236:237], s[84:85] op_sel_hi:[1,1,0]
	s_nop 0
	v_pk_fma_f32 v[238:239], v[238:239], v[236:237], s[86:87] op_sel_hi:[1,1,0]
	s_nop 0
	v_pk_mul_f32 v[238:239], v[238:239], v[236:237]
	s_nop 0
	v_pk_fma_f32 v[238:239], v[238:239], v[234:235], 1.0 op_sel_hi:[1,1,0] neg_lo:[1,0,0] neg_hi:[1,0,0]
	s_nop 0
	v_fma_f32 v242, |v240|, v238, v240
	v_fma_f32 v243, |v241|, v239, v241
	v_cvt_pk_f16_f32 v244, v242, v243
	v_pk_mul_f32 v[234:235], v[48:49], v[48:49]
	v_fma_f32 v236, |v48|, s76, 1.0
	v_fma_f32 v237, |v49|, s76, 1.0
	v_pk_mul_f32 v[234:235], v[234:235], s[78:79] op_sel_hi:[1,0]
	v_rcp_f32_e32 v236, v236
	v_rcp_f32_e32 v237, v237
	v_exp_f32_e32 v234, v234
	v_exp_f32_e32 v235, v235
	v_pk_fma_f32 v[238:239], v[236:237], s[80:81], v[248:249] op_sel_hi:[1,0,1]
	v_pk_mul_f32 v[240:241], v[232:233], v[48:49] op_sel_hi:[0,1]
	v_pk_fma_f32 v[238:239], v[238:239], v[236:237], s[82:83] op_sel_hi:[1,1,0]
	s_nop 0
	v_pk_fma_f32 v[238:239], v[238:239], v[236:237], s[84:85] op_sel_hi:[1,1,0]
	s_nop 0
	v_pk_fma_f32 v[238:239], v[238:239], v[236:237], s[86:87] op_sel_hi:[1,1,0]
	s_nop 0
	v_pk_mul_f32 v[238:239], v[238:239], v[236:237]
	s_nop 0
	v_pk_fma_f32 v[238:239], v[238:239], v[234:235], 1.0 op_sel_hi:[1,1,0] neg_lo:[1,0,0] neg_hi:[1,0,0]
	s_nop 0
	v_fma_f32 v242, |v240|, v238, v240
	v_fma_f32 v243, |v241|, v239, v241
	v_cvt_pk_f16_f32 v245, v242, v243
	v_pk_mul_f32 v[234:235], v[42:43], v[42:43]
	v_fma_f32 v236, |v42|, s76, 1.0
	v_fma_f32 v237, |v43|, s76, 1.0
	v_pk_mul_f32 v[234:235], v[234:235], s[78:79] op_sel_hi:[1,0]
	v_rcp_f32_e32 v236, v236
	v_rcp_f32_e32 v237, v237
	v_exp_f32_e32 v234, v234
	v_exp_f32_e32 v235, v235
	v_pk_fma_f32 v[238:239], v[236:237], s[80:81], v[248:249] op_sel_hi:[1,0,1]
	v_pk_mul_f32 v[240:241], v[232:233], v[42:43] op_sel_hi:[0,1]
	v_pk_fma_f32 v[238:239], v[238:239], v[236:237], s[82:83] op_sel_hi:[1,1,0]
	s_nop 0
	v_pk_fma_f32 v[238:239], v[238:239], v[236:237], s[84:85] op_sel_hi:[1,1,0]
	s_nop 0
	v_pk_fma_f32 v[238:239], v[238:239], v[236:237], s[86:87] op_sel_hi:[1,1,0]
	s_nop 0
	v_pk_mul_f32 v[238:239], v[238:239], v[236:237]
	s_nop 0
	v_pk_fma_f32 v[238:239], v[238:239], v[234:235], 1.0 op_sel_hi:[1,1,0] neg_lo:[1,0,0] neg_hi:[1,0,0]
	s_nop 0
	v_fma_f32 v242, |v240|, v238, v240
	v_fma_f32 v243, |v241|, v239, v241
	v_cvt_pk_f16_f32 v246, v242, v243
	v_pk_mul_f32 v[234:235], v[44:45], v[44:45]
	v_fma_f32 v236, |v44|, s76, 1.0
	v_fma_f32 v237, |v45|, s76, 1.0
	v_pk_mul_f32 v[234:235], v[234:235], s[78:79] op_sel_hi:[1,0]
	v_rcp_f32_e32 v236, v236
	v_rcp_f32_e32 v237, v237
	v_exp_f32_e32 v234, v234
	v_exp_f32_e32 v235, v235
	v_pk_fma_f32 v[238:239], v[236:237], s[80:81], v[248:249] op_sel_hi:[1,0,1]
	v_pk_mul_f32 v[240:241], v[232:233], v[44:45] op_sel_hi:[0,1]
	v_pk_fma_f32 v[238:239], v[238:239], v[236:237], s[82:83] op_sel_hi:[1,1,0]
	s_nop 0
	v_pk_fma_f32 v[238:239], v[238:239], v[236:237], s[84:85] op_sel_hi:[1,1,0]
	s_nop 0
	v_pk_fma_f32 v[238:239], v[238:239], v[236:237], s[86:87] op_sel_hi:[1,1,0]
	s_nop 0
	v_pk_mul_f32 v[238:239], v[238:239], v[236:237]
	s_nop 0
	v_pk_fma_f32 v[238:239], v[238:239], v[234:235], 1.0 op_sel_hi:[1,1,0] neg_lo:[1,0,0] neg_hi:[1,0,0]
	s_nop 0
	v_fma_f32 v242, |v240|, v238, v240
	v_fma_f32 v243, |v241|, v239, v241
	v_cvt_pk_f16_f32 v247, v242, v243
	v_cmp_lt_i32_e32 vcc, -1, v206
	s_nop 0
	v_permlane16_swap_b32_e32 v244, v246
	v_permlane16_swap_b32_e32 v245, v247
	s_and_saveexec_b64 s[10:11], vcc
	s_cbranch_execz .Lep_3
	v_mov_b32_e32 v250, v206
	v_mov_b32_e32 v251, 0
	v_lshlrev_b64 v[250:251], 10, v[250:251]
	v_lshl_add_u64 v[250:251], v[78:79], 0, v[250:251]
	global_store_dwordx4 v[250:251], v[244:247], off sc1
.Lep_3:
	s_or_b64 exec, exec, s[10:11]
	v_mul_f32_e32 v232, 0.5, v204
	v_pk_mul_f32 v[234:235], v[38:39], v[38:39]
	v_fma_f32 v236, |v38|, s76, 1.0
	v_fma_f32 v237, |v39|, s76, 1.0
	v_pk_mul_f32 v[234:235], v[234:235], s[78:79] op_sel_hi:[1,0]
	v_rcp_f32_e32 v236, v236
	v_rcp_f32_e32 v237, v237
	v_exp_f32_e32 v234, v234
	v_exp_f32_e32 v235, v235
	v_pk_fma_f32 v[238:239], v[236:237], s[80:81], v[248:249] op_sel_hi:[1,0,1]
	v_pk_mul_f32 v[240:241], v[232:233], v[38:39] op_sel_hi:[0,1]
	v_pk_fma_f32 v[238:239], v[238:239], v[236:237], s[82:83] op_sel_hi:[1,1,0]
	s_nop 0
	v_pk_fma_f32 v[238:239], v[238:239], v[236:237], s[84:85] op_sel_hi:[1,1,0]
	s_nop 0
	v_pk_fma_f32 v[238:239], v[238:239], v[236:237], s[86:87] op_sel_hi:[1,1,0]
	s_nop 0
	v_pk_mul_f32 v[238:239], v[238:239], v[236:237]
	s_nop 0
	v_pk_fma_f32 v[238:239], v[238:239], v[234:235], 1.0 op_sel_hi:[1,1,0] neg_lo:[1,0,0] neg_hi:[1,0,0]
	s_nop 0
	v_fma_f32 v242, |v240|, v238, v240
	v_fma_f32 v243, |v241|, v239, v241
	v_cvt_pk_f16_f32 v244, v242, v243
	v_pk_mul_f32 v[234:235], v[40:41], v[40:41]
	v_fma_f32 v236, |v40|, s76, 1.0
	v_fma_f32 v237, |v41|, s76, 1.0
	v_pk_mul_f32 v[234:235], v[234:235], s[78:79] op_sel_hi:[1,0]
	v_rcp_f32_e32 v236, v236
	v_rcp_f32_e32 v237, v237
	v_exp_f32_e32 v234, v234
	v_exp_f32_e32 v235, v235
	v_pk_fma_f32 v[238:239], v[236:237], s[80:81], v[248:249] op_sel_hi:[1,0,1]
	v_pk_mul_f32 v[240:241], v[232:233], v[40:41] op_sel_hi:[0,1]
	v_pk_fma_f32 v[238:239], v[238:239], v[236:237], s[82:83] op_sel_hi:[1,1,0]
	s_nop 0
	v_pk_fma_f32 v[238:239], v[238:239], v[236:237], s[84:85] op_sel_hi:[1,1,0]
	s_nop 0
	v_pk_fma_f32 v[238:239], v[238:239], v[236:237], s[86:87] op_sel_hi:[1,1,0]
	s_nop 0
	v_pk_mul_f32 v[238:239], v[238:239], v[236:237]
	s_nop 0
	v_pk_fma_f32 v[238:239], v[238:239], v[234:235], 1.0 op_sel_hi:[1,1,0] neg_lo:[1,0,0] neg_hi:[1,0,0]
	s_nop 0
	v_fma_f32 v242, |v240|, v238, v240
	v_fma_f32 v243, |v241|, v239, v241
	v_cvt_pk_f16_f32 v245, v242, v243
	v_pk_mul_f32 v[234:235], v[34:35], v[34:35]
	v_fma_f32 v236, |v34|, s76, 1.0
	v_fma_f32 v237, |v35|, s76, 1.0
	v_pk_mul_f32 v[234:235], v[234:235], s[78:79] op_sel_hi:[1,0]
	v_rcp_f32_e32 v236, v236
	v_rcp_f32_e32 v237, v237
	v_exp_f32_e32 v234, v234
	v_exp_f32_e32 v235, v235
	v_pk_fma_f32 v[238:239], v[236:237], s[80:81], v[248:249] op_sel_hi:[1,0,1]
	v_pk_mul_f32 v[240:241], v[232:233], v[34:35] op_sel_hi:[0,1]
	v_pk_fma_f32 v[238:239], v[238:239], v[236:237], s[82:83] op_sel_hi:[1,1,0]
	s_nop 0
	v_pk_fma_f32 v[238:239], v[238:239], v[236:237], s[84:85] op_sel_hi:[1,1,0]
	s_nop 0
	v_pk_fma_f32 v[238:239], v[238:239], v[236:237], s[86:87] op_sel_hi:[1,1,0]
	s_nop 0
	v_pk_mul_f32 v[238:239], v[238:239], v[236:237]
	s_nop 0
	v_pk_fma_f32 v[238:239], v[238:239], v[234:235], 1.0 op_sel_hi:[1,1,0] neg_lo:[1,0,0] neg_hi:[1,0,0]
	s_nop 0
	v_fma_f32 v242, |v240|, v238, v240
	v_fma_f32 v243, |v241|, v239, v241
	v_cvt_pk_f16_f32 v246, v242, v243
	v_pk_mul_f32 v[234:235], v[36:37], v[36:37]
	v_fma_f32 v236, |v36|, s76, 1.0
	v_fma_f32 v237, |v37|, s76, 1.0
	v_pk_mul_f32 v[234:235], v[234:235], s[78:79] op_sel_hi:[1,0]
	v_rcp_f32_e32 v236, v236
	v_rcp_f32_e32 v237, v237
	v_exp_f32_e32 v234, v234
	v_exp_f32_e32 v235, v235
	v_pk_fma_f32 v[238:239], v[236:237], s[80:81], v[248:249] op_sel_hi:[1,0,1]
	v_pk_mul_f32 v[240:241], v[232:233], v[36:37] op_sel_hi:[0,1]
	v_pk_fma_f32 v[238:239], v[238:239], v[236:237], s[82:83] op_sel_hi:[1,1,0]
	s_nop 0
	v_pk_fma_f32 v[238:239], v[238:239], v[236:237], s[84:85] op_sel_hi:[1,1,0]
	s_nop 0
	v_pk_fma_f32 v[238:239], v[238:239], v[236:237], s[86:87] op_sel_hi:[1,1,0]
	s_nop 0
	v_pk_mul_f32 v[238:239], v[238:239], v[236:237]
	s_nop 0
	v_pk_fma_f32 v[238:239], v[238:239], v[234:235], 1.0 op_sel_hi:[1,1,0] neg_lo:[1,0,0] neg_hi:[1,0,0]
	s_nop 0
	v_fma_f32 v242, |v240|, v238, v240
	v_fma_f32 v243, |v241|, v239, v241
	v_cvt_pk_f16_f32 v247, v242, v243
	v_cmp_lt_i32_e32 vcc, -1, v202
	s_nop 0
	v_permlane16_swap_b32_e32 v244, v246
	v_permlane16_swap_b32_e32 v245, v247
	s_and_saveexec_b64 s[10:11], vcc
	s_cbranch_execz .Lep_4
	v_mov_b32_e32 v250, v202
	v_mov_b32_e32 v251, 0
	v_lshlrev_b64 v[250:251], 10, v[250:251]
	v_lshl_add_u64 v[250:251], v[78:79], 0, v[250:251]
	global_store_dwordx4 v[250:251], v[244:247], off sc1
.Lep_4:
	s_or_b64 exec, exec, s[10:11]
	v_mul_f32_e32 v232, 0.5, v200
	v_pk_mul_f32 v[234:235], v[30:31], v[30:31]
	v_fma_f32 v236, |v30|, s76, 1.0
	v_fma_f32 v237, |v31|, s76, 1.0
	v_pk_mul_f32 v[234:235], v[234:235], s[78:79] op_sel_hi:[1,0]
	v_rcp_f32_e32 v236, v236
	v_rcp_f32_e32 v237, v237
	v_exp_f32_e32 v234, v234
	v_exp_f32_e32 v235, v235
	v_pk_fma_f32 v[238:239], v[236:237], s[80:81], v[248:249] op_sel_hi:[1,0,1]
	v_pk_mul_f32 v[240:241], v[232:233], v[30:31] op_sel_hi:[0,1]
	v_pk_fma_f32 v[238:239], v[238:239], v[236:237], s[82:83] op_sel_hi:[1,1,0]
	s_nop 0
	v_pk_fma_f32 v[238:239], v[238:239], v[236:237], s[84:85] op_sel_hi:[1,1,0]
	s_nop 0
	v_pk_fma_f32 v[238:239], v[238:239], v[236:237], s[86:87] op_sel_hi:[1,1,0]
	s_nop 0
	v_pk_mul_f32 v[238:239], v[238:239], v[236:237]
	s_nop 0
	v_pk_fma_f32 v[238:239], v[238:239], v[234:235], 1.0 op_sel_hi:[1,1,0] neg_lo:[1,0,0] neg_hi:[1,0,0]
	s_nop 0
	v_fma_f32 v242, |v240|, v238, v240
	v_fma_f32 v243, |v241|, v239, v241
	v_cvt_pk_f16_f32 v244, v242, v243
	v_pk_mul_f32 v[234:235], v[32:33], v[32:33]
	v_fma_f32 v236, |v32|, s76, 1.0
	v_fma_f32 v237, |v33|, s76, 1.0
	v_pk_mul_f32 v[234:235], v[234:235], s[78:79] op_sel_hi:[1,0]
	v_rcp_f32_e32 v236, v236
	v_rcp_f32_e32 v237, v237
	v_exp_f32_e32 v234, v234
	v_exp_f32_e32 v235, v235
	v_pk_fma_f32 v[238:239], v[236:237], s[80:81], v[248:249] op_sel_hi:[1,0,1]
	v_pk_mul_f32 v[240:241], v[232:233], v[32:33] op_sel_hi:[0,1]
	v_pk_fma_f32 v[238:239], v[238:239], v[236:237], s[82:83] op_sel_hi:[1,1,0]
	s_nop 0
	v_pk_fma_f32 v[238:239], v[238:239], v[236:237], s[84:85] op_sel_hi:[1,1,0]
	s_nop 0
	v_pk_fma_f32 v[238:239], v[238:239], v[236:237], s[86:87] op_sel_hi:[1,1,0]
	s_nop 0
	v_pk_mul_f32 v[238:239], v[238:239], v[236:237]
	s_nop 0
	v_pk_fma_f32 v[238:239], v[238:239], v[234:235], 1.0 op_sel_hi:[1,1,0] neg_lo:[1,0,0] neg_hi:[1,0,0]
	s_nop 0
	v_fma_f32 v242, |v240|, v238, v240
	v_fma_f32 v243, |v241|, v239, v241
	v_cvt_pk_f16_f32 v245, v242, v243
	v_pk_mul_f32 v[234:235], v[26:27], v[26:27]
	v_fma_f32 v236, |v26|, s76, 1.0
	v_fma_f32 v237, |v27|, s76, 1.0
	v_pk_mul_f32 v[234:235], v[234:235], s[78:79] op_sel_hi:[1,0]
	v_rcp_f32_e32 v236, v236
	v_rcp_f32_e32 v237, v237
	v_exp_f32_e32 v234, v234
	v_exp_f32_e32 v235, v235
	v_pk_fma_f32 v[238:239], v[236:237], s[80:81], v[248:249] op_sel_hi:[1,0,1]
	v_pk_mul_f32 v[240:241], v[232:233], v[26:27] op_sel_hi:[0,1]
	v_pk_fma_f32 v[238:239], v[238:239], v[236:237], s[82:83] op_sel_hi:[1,1,0]
	s_nop 0
	v_pk_fma_f32 v[238:239], v[238:239], v[236:237], s[84:85] op_sel_hi:[1,1,0]
	s_nop 0
	v_pk_fma_f32 v[238:239], v[238:239], v[236:237], s[86:87] op_sel_hi:[1,1,0]
	s_nop 0
	v_pk_mul_f32 v[238:239], v[238:239], v[236:237]
	s_nop 0
	v_pk_fma_f32 v[238:239], v[238:239], v[234:235], 1.0 op_sel_hi:[1,1,0] neg_lo:[1,0,0] neg_hi:[1,0,0]
	s_nop 0
	v_fma_f32 v242, |v240|, v238, v240
	v_fma_f32 v243, |v241|, v239, v241
	v_cvt_pk_f16_f32 v246, v242, v243
	v_pk_mul_f32 v[234:235], v[28:29], v[28:29]
	v_fma_f32 v236, |v28|, s76, 1.0
	v_fma_f32 v237, |v29|, s76, 1.0
	v_pk_mul_f32 v[234:235], v[234:235], s[78:79] op_sel_hi:[1,0]
	v_rcp_f32_e32 v236, v236
	v_rcp_f32_e32 v237, v237
	v_exp_f32_e32 v234, v234
	v_exp_f32_e32 v235, v235
	v_pk_fma_f32 v[238:239], v[236:237], s[80:81], v[248:249] op_sel_hi:[1,0,1]
	v_pk_mul_f32 v[240:241], v[232:233], v[28:29] op_sel_hi:[0,1]
	v_pk_fma_f32 v[238:239], v[238:239], v[236:237], s[82:83] op_sel_hi:[1,1,0]
	s_nop 0
	v_pk_fma_f32 v[238:239], v[238:239], v[236:237], s[84:85] op_sel_hi:[1,1,0]
	s_nop 0
	v_pk_fma_f32 v[238:239], v[238:239], v[236:237], s[86:87] op_sel_hi:[1,1,0]
	s_nop 0
	v_pk_mul_f32 v[238:239], v[238:239], v[236:237]
	s_nop 0
	v_pk_fma_f32 v[238:239], v[238:239], v[234:235], 1.0 op_sel_hi:[1,1,0] neg_lo:[1,0,0] neg_hi:[1,0,0]
	s_nop 0
	v_fma_f32 v242, |v240|, v238, v240
	v_fma_f32 v243, |v241|, v239, v241
	v_cvt_pk_f16_f32 v247, v242, v243
	v_cmp_lt_i32_e32 vcc, -1, v198
	s_nop 0
	v_permlane16_swap_b32_e32 v244, v246
	v_permlane16_swap_b32_e32 v245, v247
	s_and_saveexec_b64 s[10:11], vcc
	s_cbranch_execz .Lep_5
	v_mov_b32_e32 v250, v198
	v_mov_b32_e32 v251, 0
	v_lshlrev_b64 v[250:251], 10, v[250:251]
	v_lshl_add_u64 v[250:251], v[78:79], 0, v[250:251]
	global_store_dwordx4 v[250:251], v[244:247], off sc1
.Lep_5:
	s_or_b64 exec, exec, s[10:11]
	v_mul_f32_e32 v232, 0.5, v196
	v_pk_mul_f32 v[234:235], v[22:23], v[22:23]
	v_fma_f32 v236, |v22|, s76, 1.0
	v_fma_f32 v237, |v23|, s76, 1.0
	v_pk_mul_f32 v[234:235], v[234:235], s[78:79] op_sel_hi:[1,0]
	v_rcp_f32_e32 v236, v236
	v_rcp_f32_e32 v237, v237
	v_exp_f32_e32 v234, v234
	v_exp_f32_e32 v235, v235
	v_pk_fma_f32 v[238:239], v[236:237], s[80:81], v[248:249] op_sel_hi:[1,0,1]
	v_pk_mul_f32 v[240:241], v[232:233], v[22:23] op_sel_hi:[0,1]
	v_pk_fma_f32 v[238:239], v[238:239], v[236:237], s[82:83] op_sel_hi:[1,1,0]
	s_nop 0
	v_pk_fma_f32 v[238:239], v[238:239], v[236:237], s[84:85] op_sel_hi:[1,1,0]
	s_nop 0
	v_pk_fma_f32 v[238:239], v[238:239], v[236:237], s[86:87] op_sel_hi:[1,1,0]
	s_nop 0
	v_pk_mul_f32 v[238:239], v[238:239], v[236:237]
	s_nop 0
	v_pk_fma_f32 v[238:239], v[238:239], v[234:235], 1.0 op_sel_hi:[1,1,0] neg_lo:[1,0,0] neg_hi:[1,0,0]
	s_nop 0
	v_fma_f32 v242, |v240|, v238, v240
	v_fma_f32 v243, |v241|, v239, v241
	v_cvt_pk_f16_f32 v244, v242, v243
	v_pk_mul_f32 v[234:235], v[24:25], v[24:25]
	v_fma_f32 v236, |v24|, s76, 1.0
	v_fma_f32 v237, |v25|, s76, 1.0
	v_pk_mul_f32 v[234:235], v[234:235], s[78:79] op_sel_hi:[1,0]
	v_rcp_f32_e32 v236, v236
	v_rcp_f32_e32 v237, v237
	v_exp_f32_e32 v234, v234
	v_exp_f32_e32 v235, v235
	v_pk_fma_f32 v[238:239], v[236:237], s[80:81], v[248:249] op_sel_hi:[1,0,1]
	v_pk_mul_f32 v[240:241], v[232:233], v[24:25] op_sel_hi:[0,1]
	v_pk_fma_f32 v[238:239], v[238:239], v[236:237], s[82:83] op_sel_hi:[1,1,0]
	s_nop 0
	v_pk_fma_f32 v[238:239], v[238:239], v[236:237], s[84:85] op_sel_hi:[1,1,0]
	s_nop 0
	v_pk_fma_f32 v[238:239], v[238:239], v[236:237], s[86:87] op_sel_hi:[1,1,0]
	s_nop 0
	v_pk_mul_f32 v[238:239], v[238:239], v[236:237]
	s_nop 0
	v_pk_fma_f32 v[238:239], v[238:239], v[234:235], 1.0 op_sel_hi:[1,1,0] neg_lo:[1,0,0] neg_hi:[1,0,0]
	s_nop 0
	v_fma_f32 v242, |v240|, v238, v240
	v_fma_f32 v243, |v241|, v239, v241
	v_cvt_pk_f16_f32 v245, v242, v243
	v_pk_mul_f32 v[234:235], v[18:19], v[18:19]
	v_fma_f32 v236, |v18|, s76, 1.0
	v_fma_f32 v237, |v19|, s76, 1.0
	v_pk_mul_f32 v[234:235], v[234:235], s[78:79] op_sel_hi:[1,0]
	v_rcp_f32_e32 v236, v236
	v_rcp_f32_e32 v237, v237
	v_exp_f32_e32 v234, v234
	v_exp_f32_e32 v235, v235
	v_pk_fma_f32 v[238:239], v[236:237], s[80:81], v[248:249] op_sel_hi:[1,0,1]
	v_pk_mul_f32 v[240:241], v[232:233], v[18:19] op_sel_hi:[0,1]
	v_pk_fma_f32 v[238:239], v[238:239], v[236:237], s[82:83] op_sel_hi:[1,1,0]
	s_nop 0
	v_pk_fma_f32 v[238:239], v[238:239], v[236:237], s[84:85] op_sel_hi:[1,1,0]
	s_nop 0
	v_pk_fma_f32 v[238:239], v[238:239], v[236:237], s[86:87] op_sel_hi:[1,1,0]
	s_nop 0
	v_pk_mul_f32 v[238:239], v[238:239], v[236:237]
	s_nop 0
	v_pk_fma_f32 v[238:239], v[238:239], v[234:235], 1.0 op_sel_hi:[1,1,0] neg_lo:[1,0,0] neg_hi:[1,0,0]
	s_nop 0
	v_fma_f32 v242, |v240|, v238, v240
	v_fma_f32 v243, |v241|, v239, v241
	v_cvt_pk_f16_f32 v246, v242, v243
	v_pk_mul_f32 v[234:235], v[20:21], v[20:21]
	v_fma_f32 v236, |v20|, s76, 1.0
	v_fma_f32 v237, |v21|, s76, 1.0
	v_pk_mul_f32 v[234:235], v[234:235], s[78:79] op_sel_hi:[1,0]
	v_rcp_f32_e32 v236, v236
	v_rcp_f32_e32 v237, v237
	v_exp_f32_e32 v234, v234
	v_exp_f32_e32 v235, v235
	v_pk_fma_f32 v[238:239], v[236:237], s[80:81], v[248:249] op_sel_hi:[1,0,1]
	v_pk_mul_f32 v[240:241], v[232:233], v[20:21] op_sel_hi:[0,1]
	v_pk_fma_f32 v[238:239], v[238:239], v[236:237], s[82:83] op_sel_hi:[1,1,0]
	s_nop 0
	v_pk_fma_f32 v[238:239], v[238:239], v[236:237], s[84:85] op_sel_hi:[1,1,0]
	s_nop 0
	v_pk_fma_f32 v[238:239], v[238:239], v[236:237], s[86:87] op_sel_hi:[1,1,0]
	s_nop 0
	v_pk_mul_f32 v[238:239], v[238:239], v[236:237]
	s_nop 0
	v_pk_fma_f32 v[238:239], v[238:239], v[234:235], 1.0 op_sel_hi:[1,1,0] neg_lo:[1,0,0] neg_hi:[1,0,0]
	s_nop 0
	v_fma_f32 v242, |v240|, v238, v240
	v_fma_f32 v243, |v241|, v239, v241
	v_cvt_pk_f16_f32 v247, v242, v243
	v_cmp_lt_i32_e32 vcc, -1, v194
	s_nop 0
	v_permlane16_swap_b32_e32 v244, v246
	v_permlane16_swap_b32_e32 v245, v247
	s_and_saveexec_b64 s[10:11], vcc
	s_cbranch_execz .Lep_6
	v_mov_b32_e32 v250, v194
	v_mov_b32_e32 v251, 0
	v_lshlrev_b64 v[250:251], 10, v[250:251]
	v_lshl_add_u64 v[250:251], v[78:79], 0, v[250:251]
	global_store_dwordx4 v[250:251], v[244:247], off sc1
.Lep_6:
	s_or_b64 exec, exec, s[10:11]
	v_mul_f32_e32 v232, 0.5, v192
	v_pk_mul_f32 v[234:235], v[14:15], v[14:15]
	v_fma_f32 v236, |v14|, s76, 1.0
	v_fma_f32 v237, |v15|, s76, 1.0
	v_pk_mul_f32 v[234:235], v[234:235], s[78:79] op_sel_hi:[1,0]
	v_rcp_f32_e32 v236, v236
	v_rcp_f32_e32 v237, v237
	v_exp_f32_e32 v234, v234
	v_exp_f32_e32 v235, v235
	v_pk_fma_f32 v[238:239], v[236:237], s[80:81], v[248:249] op_sel_hi:[1,0,1]
	v_pk_mul_f32 v[240:241], v[232:233], v[14:15] op_sel_hi:[0,1]
	v_pk_fma_f32 v[238:239], v[238:239], v[236:237], s[82:83] op_sel_hi:[1,1,0]
	s_nop 0
	v_pk_fma_f32 v[238:239], v[238:239], v[236:237], s[84:85] op_sel_hi:[1,1,0]
	s_nop 0
	v_pk_fma_f32 v[238:239], v[238:239], v[236:237], s[86:87] op_sel_hi:[1,1,0]
	s_nop 0
	v_pk_mul_f32 v[238:239], v[238:239], v[236:237]
	s_nop 0
	v_pk_fma_f32 v[238:239], v[238:239], v[234:235], 1.0 op_sel_hi:[1,1,0] neg_lo:[1,0,0] neg_hi:[1,0,0]
	s_nop 0
	v_fma_f32 v242, |v240|, v238, v240
	v_fma_f32 v243, |v241|, v239, v241
	v_cvt_pk_f16_f32 v244, v242, v243
	v_pk_mul_f32 v[234:235], v[16:17], v[16:17]
	v_fma_f32 v236, |v16|, s76, 1.0
	v_fma_f32 v237, |v17|, s76, 1.0
	v_pk_mul_f32 v[234:235], v[234:235], s[78:79] op_sel_hi:[1,0]
	v_rcp_f32_e32 v236, v236
	v_rcp_f32_e32 v237, v237
	v_exp_f32_e32 v234, v234
	v_exp_f32_e32 v235, v235
	v_pk_fma_f32 v[238:239], v[236:237], s[80:81], v[248:249] op_sel_hi:[1,0,1]
	v_pk_mul_f32 v[240:241], v[232:233], v[16:17] op_sel_hi:[0,1]
	v_pk_fma_f32 v[238:239], v[238:239], v[236:237], s[82:83] op_sel_hi:[1,1,0]
	s_nop 0
	v_pk_fma_f32 v[238:239], v[238:239], v[236:237], s[84:85] op_sel_hi:[1,1,0]
	s_nop 0
	v_pk_fma_f32 v[238:239], v[238:239], v[236:237], s[86:87] op_sel_hi:[1,1,0]
	s_nop 0
	v_pk_mul_f32 v[238:239], v[238:239], v[236:237]
	s_nop 0
	v_pk_fma_f32 v[238:239], v[238:239], v[234:235], 1.0 op_sel_hi:[1,1,0] neg_lo:[1,0,0] neg_hi:[1,0,0]
	s_nop 0
	v_fma_f32 v242, |v240|, v238, v240
	v_fma_f32 v243, |v241|, v239, v241
	v_cvt_pk_f16_f32 v245, v242, v243
	v_pk_mul_f32 v[234:235], v[10:11], v[10:11]
	v_fma_f32 v236, |v10|, s76, 1.0
	v_fma_f32 v237, |v11|, s76, 1.0
	v_pk_mul_f32 v[234:235], v[234:235], s[78:79] op_sel_hi:[1,0]
	v_rcp_f32_e32 v236, v236
	v_rcp_f32_e32 v237, v237
	v_exp_f32_e32 v234, v234
	v_exp_f32_e32 v235, v235
	v_pk_fma_f32 v[238:239], v[236:237], s[80:81], v[248:249] op_sel_hi:[1,0,1]
	v_pk_mul_f32 v[240:241], v[232:233], v[10:11] op_sel_hi:[0,1]
	v_pk_fma_f32 v[238:239], v[238:239], v[236:237], s[82:83] op_sel_hi:[1,1,0]
	s_nop 0
	v_pk_fma_f32 v[238:239], v[238:239], v[236:237], s[84:85] op_sel_hi:[1,1,0]
	s_nop 0
	v_pk_fma_f32 v[238:239], v[238:239], v[236:237], s[86:87] op_sel_hi:[1,1,0]
	s_nop 0
	v_pk_mul_f32 v[238:239], v[238:239], v[236:237]
	s_nop 0
	v_pk_fma_f32 v[238:239], v[238:239], v[234:235], 1.0 op_sel_hi:[1,1,0] neg_lo:[1,0,0] neg_hi:[1,0,0]
	s_nop 0
	v_fma_f32 v242, |v240|, v238, v240
	v_fma_f32 v243, |v241|, v239, v241
	v_cvt_pk_f16_f32 v246, v242, v243
	v_pk_mul_f32 v[234:235], v[12:13], v[12:13]
	v_fma_f32 v236, |v12|, s76, 1.0
	v_fma_f32 v237, |v13|, s76, 1.0
	v_pk_mul_f32 v[234:235], v[234:235], s[78:79] op_sel_hi:[1,0]
	v_rcp_f32_e32 v236, v236
	v_rcp_f32_e32 v237, v237
	v_exp_f32_e32 v234, v234
	v_exp_f32_e32 v235, v235
	v_pk_fma_f32 v[238:239], v[236:237], s[80:81], v[248:249] op_sel_hi:[1,0,1]
	v_pk_mul_f32 v[240:241], v[232:233], v[12:13] op_sel_hi:[0,1]
	v_pk_fma_f32 v[238:239], v[238:239], v[236:237], s[82:83] op_sel_hi:[1,1,0]
	s_nop 0
	v_pk_fma_f32 v[238:239], v[238:239], v[236:237], s[84:85] op_sel_hi:[1,1,0]
	s_nop 0
	v_pk_fma_f32 v[238:239], v[238:239], v[236:237], s[86:87] op_sel_hi:[1,1,0]
	s_nop 0
	v_pk_mul_f32 v[238:239], v[238:239], v[236:237]
	s_nop 0
	v_pk_fma_f32 v[238:239], v[238:239], v[234:235], 1.0 op_sel_hi:[1,1,0] neg_lo:[1,0,0] neg_hi:[1,0,0]
	s_nop 0
	v_fma_f32 v242, |v240|, v238, v240
	v_fma_f32 v243, |v241|, v239, v241
	v_cvt_pk_f16_f32 v247, v242, v243
	v_cmp_lt_i32_e32 vcc, -1, v190
	s_nop 0
	v_permlane16_swap_b32_e32 v244, v246
	v_permlane16_swap_b32_e32 v245, v247
	s_and_saveexec_b64 s[10:11], vcc
	s_cbranch_execz .Lep_7
	v_mov_b32_e32 v250, v190
	v_mov_b32_e32 v251, 0
	v_lshlrev_b64 v[250:251], 10, v[250:251]
	v_lshl_add_u64 v[250:251], v[78:79], 0, v[250:251]
	global_store_dwordx4 v[250:251], v[244:247], off sc1
.Lep_7:
	s_or_b64 exec, exec, s[10:11]
	v_mul_f32_e32 v232, 0.5, v188
	v_pk_mul_f32 v[234:235], v[6:7], v[6:7]
	v_fma_f32 v236, |v6|, s76, 1.0
	v_fma_f32 v237, |v7|, s76, 1.0
	v_pk_mul_f32 v[234:235], v[234:235], s[78:79] op_sel_hi:[1,0]
	v_rcp_f32_e32 v236, v236
	v_rcp_f32_e32 v237, v237
	v_exp_f32_e32 v234, v234
	v_exp_f32_e32 v235, v235
	v_pk_fma_f32 v[238:239], v[236:237], s[80:81], v[248:249] op_sel_hi:[1,0,1]
	v_pk_mul_f32 v[240:241], v[232:233], v[6:7] op_sel_hi:[0,1]
	v_pk_fma_f32 v[238:239], v[238:239], v[236:237], s[82:83] op_sel_hi:[1,1,0]
	s_nop 0
	v_pk_fma_f32 v[238:239], v[238:239], v[236:237], s[84:85] op_sel_hi:[1,1,0]
	s_nop 0
	v_pk_fma_f32 v[238:239], v[238:239], v[236:237], s[86:87] op_sel_hi:[1,1,0]
	s_nop 0
	v_pk_mul_f32 v[238:239], v[238:239], v[236:237]
	s_nop 0
	v_pk_fma_f32 v[238:239], v[238:239], v[234:235], 1.0 op_sel_hi:[1,1,0] neg_lo:[1,0,0] neg_hi:[1,0,0]
	s_nop 0
	v_fma_f32 v242, |v240|, v238, v240
	v_fma_f32 v243, |v241|, v239, v241
	v_cvt_pk_f16_f32 v244, v242, v243
	v_pk_mul_f32 v[234:235], v[8:9], v[8:9]
	v_fma_f32 v236, |v8|, s76, 1.0
	v_fma_f32 v237, |v9|, s76, 1.0
	v_pk_mul_f32 v[234:235], v[234:235], s[78:79] op_sel_hi:[1,0]
	v_rcp_f32_e32 v236, v236
	v_rcp_f32_e32 v237, v237
	v_exp_f32_e32 v234, v234
	v_exp_f32_e32 v235, v235
	v_pk_fma_f32 v[238:239], v[236:237], s[80:81], v[248:249] op_sel_hi:[1,0,1]
	v_pk_mul_f32 v[240:241], v[232:233], v[8:9] op_sel_hi:[0,1]
	v_pk_fma_f32 v[238:239], v[238:239], v[236:237], s[82:83] op_sel_hi:[1,1,0]
	s_nop 0
	v_pk_fma_f32 v[238:239], v[238:239], v[236:237], s[84:85] op_sel_hi:[1,1,0]
	s_nop 0
	v_pk_fma_f32 v[238:239], v[238:239], v[236:237], s[86:87] op_sel_hi:[1,1,0]
	s_nop 0
	v_pk_mul_f32 v[238:239], v[238:239], v[236:237]
	s_nop 0
	v_pk_fma_f32 v[238:239], v[238:239], v[234:235], 1.0 op_sel_hi:[1,1,0] neg_lo:[1,0,0] neg_hi:[1,0,0]
	s_nop 0
	v_fma_f32 v242, |v240|, v238, v240
	v_fma_f32 v243, |v241|, v239, v241
	v_cvt_pk_f16_f32 v245, v242, v243
	v_pk_mul_f32 v[234:235], v[2:3], v[2:3]
	v_fma_f32 v236, |v2|, s76, 1.0
	v_fma_f32 v237, |v3|, s76, 1.0
	v_pk_mul_f32 v[234:235], v[234:235], s[78:79] op_sel_hi:[1,0]
	v_rcp_f32_e32 v236, v236
	v_rcp_f32_e32 v237, v237
	v_exp_f32_e32 v234, v234
	v_exp_f32_e32 v235, v235
	v_pk_fma_f32 v[238:239], v[236:237], s[80:81], v[248:249] op_sel_hi:[1,0,1]
	v_pk_mul_f32 v[240:241], v[232:233], v[2:3] op_sel_hi:[0,1]
	v_pk_fma_f32 v[238:239], v[238:239], v[236:237], s[82:83] op_sel_hi:[1,1,0]
	s_nop 0
	v_pk_fma_f32 v[238:239], v[238:239], v[236:237], s[84:85] op_sel_hi:[1,1,0]
	s_nop 0
	v_pk_fma_f32 v[238:239], v[238:239], v[236:237], s[86:87] op_sel_hi:[1,1,0]
	s_nop 0
	v_pk_mul_f32 v[238:239], v[238:239], v[236:237]
	s_nop 0
	v_pk_fma_f32 v[238:239], v[238:239], v[234:235], 1.0 op_sel_hi:[1,1,0] neg_lo:[1,0,0] neg_hi:[1,0,0]
	s_nop 0
	v_fma_f32 v242, |v240|, v238, v240
	v_fma_f32 v243, |v241|, v239, v241
	v_cvt_pk_f16_f32 v246, v242, v243
	v_pk_mul_f32 v[234:235], v[4:5], v[4:5]
	v_fma_f32 v236, |v4|, s76, 1.0
	v_fma_f32 v237, |v5|, s76, 1.0
	v_pk_mul_f32 v[234:235], v[234:235], s[78:79] op_sel_hi:[1,0]
	v_rcp_f32_e32 v236, v236
	v_rcp_f32_e32 v237, v237
	v_exp_f32_e32 v234, v234
	v_exp_f32_e32 v235, v235
	v_pk_fma_f32 v[238:239], v[236:237], s[80:81], v[248:249] op_sel_hi:[1,0,1]
	v_pk_mul_f32 v[240:241], v[232:233], v[4:5] op_sel_hi:[0,1]
	v_pk_fma_f32 v[238:239], v[238:239], v[236:237], s[82:83] op_sel_hi:[1,1,0]
	s_nop 0
	v_pk_fma_f32 v[238:239], v[238:239], v[236:237], s[84:85] op_sel_hi:[1,1,0]
	s_nop 0
	v_pk_fma_f32 v[238:239], v[238:239], v[236:237], s[86:87] op_sel_hi:[1,1,0]
	s_nop 0
	v_pk_mul_f32 v[238:239], v[238:239], v[236:237]
	s_nop 0
	v_pk_fma_f32 v[238:239], v[238:239], v[234:235], 1.0 op_sel_hi:[1,1,0] neg_lo:[1,0,0] neg_hi:[1,0,0]
	s_nop 0
	v_fma_f32 v242, |v240|, v238, v240
	v_fma_f32 v243, |v241|, v239, v241
	v_cvt_pk_f16_f32 v247, v242, v243
	v_cmp_lt_i32_e32 vcc, -1, v186
	s_nop 0
	v_permlane16_swap_b32_e32 v244, v246
	v_permlane16_swap_b32_e32 v245, v247
	s_and_saveexec_b64 s[10:11], vcc
	s_cbranch_execz .Lep_8
	v_mov_b32_e32 v250, v186
	v_mov_b32_e32 v251, 0
	v_lshlrev_b64 v[250:251], 10, v[250:251]
	v_lshl_add_u64 v[250:251], v[78:79], 0, v[250:251]
	global_store_dwordx4 v[250:251], v[244:247], off sc1
.Lep_8:
	s_or_b64 exec, exec, s[10:11]
.LBB2_132:
	s_endpgm
	.p2align	8
